# v90 + attention QK phases: exact counted lgkmcnt waits per MFMA (each QK MFMA waits only for the K-fragment ds_read it consumes) in all 5 tile loops
# speedup vs baseline: 1.0031x; 1.0016x over previous
.LBB0_3622:
	s_add_i32 s0, s0, 0
	v_add3_u32 v0, s0, v123, v124
	ds_read_b128 v[34:37], v0
	ds_read_b128 v[50:53], v0 offset:512
	ds_read_b128 v[128:131], v0 offset:2048
	ds_read_b128 v[132:135], v0 offset:2560
	s_lshl_b32 s6, s8, 6
	v_readfirstlane_b32 s7, v119
	s_or_b32 s8, s6, 63
	s_cmp_le_i32 s8, s7
	s_cselect_b64 s[8:9], -1, 0
	s_waitcnt lgkmcnt(3)
	v_mfma_f32_32x32x16_bf16 v[34:49], v[34:37], v[66:69], 0
	s_addk_i32 s7, 0xff9f
	s_cmp_gt_i32 s6, s7
	s_cselect_b64 s[10:11], -1, 0
	s_and_b64 s[8:9], s[8:9], s[10:11]
	s_and_b64 vcc, exec, s[8:9]
	s_waitcnt lgkmcnt(2)
	v_mfma_f32_32x32x16_bf16 v[50:65], v[50:53], v[66:69], 0
	ds_read_b128 v[136:139], v0 offset:4096
	ds_read_b128 v[140:143], v0 offset:4608
	s_waitcnt lgkmcnt(3)
	v_mfma_f32_32x32x16_bf16 v[34:49], v[128:131], v[70:73], v[34:49]
	s_waitcnt lgkmcnt(2)
	v_mfma_f32_32x32x16_bf16 v[50:65], v[132:135], v[70:73], v[50:65]
	ds_read_b128 v[128:131], v0 offset:6144
	ds_read_b128 v[132:135], v0 offset:6656
	s_waitcnt lgkmcnt(3)
	v_mfma_f32_32x32x16_bf16 v[34:49], v[136:139], v[74:77], v[34:49]
	s_waitcnt lgkmcnt(2)
	v_mfma_f32_32x32x16_bf16 v[50:65], v[140:143], v[74:77], v[50:65]
	s_waitcnt lgkmcnt(1)
	v_mfma_f32_32x32x16_bf16 v[34:49], v[128:131], v[78:81], v[34:49]
	s_waitcnt lgkmcnt(0)
	v_mfma_f32_32x32x16_bf16 v[50:65], v[132:135], v[78:81], v[50:65]
	s_cbranch_vccnz .LBB0_3626
	v_or_b32_e32 v0, s6, v127
	v_sub_u32_e32 v0, v119, v0
	v_subrev_u32_e32 v128, 32, v0
	v_cmp_gt_u32_e64 s[6:7], s57, v128
	v_add_u32_e32 v128, -1, v0
	v_cmp_gt_u32_e32 vcc, s57, v0
	s_nop 4
	v_cndmask_b32_e64 v50, v240, v50, s[6:7]
	v_cmp_gt_u32_e64 s[6:7], s57, v128
	v_subrev_u32_e32 v128, 33, v0
	v_cmp_gt_u32_e64 s[8:9], s57, v128
	v_add_u32_e32 v128, -2, v0
	s_nop 0
	v_cndmask_b32_e64 v51, v240, v51, s[8:9]
	v_cmp_gt_u32_e64 s[8:9], s57, v128
	v_subrev_u32_e32 v128, 34, v0
	v_cmp_gt_u32_e64 s[10:11], s57, v128
	v_add_u32_e32 v128, -3, v0
	s_nop 0
	v_cndmask_b32_e64 v52, v240, v52, s[10:11]
	v_cmp_gt_u32_e64 s[10:11], s57, v128
	v_subrev_u32_e32 v128, 35, v0
	v_cmp_gt_u32_e64 s[12:13], s57, v128
	v_add_u32_e32 v128, -8, v0
	s_nop 0
	v_cndmask_b32_e64 v53, v240, v53, s[12:13]
	v_cmp_gt_u32_e64 s[12:13], s57, v128
	v_subrev_u32_e32 v128, 40, v0
	v_cmp_gt_u32_e64 s[14:15], s57, v128
	v_add_u32_e32 v128, -9, v0
	s_nop 0
	v_cndmask_b32_e64 v54, v240, v54, s[14:15]
	v_cmp_gt_u32_e64 s[14:15], s57, v128
	v_subrev_u32_e32 v128, 41, v0
	v_cmp_gt_u32_e64 s[16:17], s57, v128
	v_add_u32_e32 v128, -10, v0
	s_nop 0
	v_cndmask_b32_e64 v55, v240, v55, s[16:17]
	v_cmp_gt_u32_e64 s[16:17], s57, v128
	v_subrev_u32_e32 v128, 42, v0
	v_cmp_gt_u32_e64 s[18:19], s57, v128
	v_add_u32_e32 v128, -11, v0
	s_nop 0
	v_cndmask_b32_e64 v56, v240, v56, s[18:19]
	v_cmp_gt_u32_e64 s[18:19], s57, v128
	v_subrev_u32_e32 v128, 43, v0
	v_cmp_gt_u32_e64 s[20:21], s57, v128
	v_add_u32_e32 v128, -16, v0
	s_nop 0
	v_cndmask_b32_e64 v57, v240, v57, s[20:21]
	v_cmp_gt_u32_e64 s[20:21], s57, v128
	v_subrev_u32_e32 v128, 48, v0
	v_cmp_gt_u32_e64 s[22:23], s57, v128
	v_subrev_u32_e32 v128, 17, v0
	s_nop 0
	v_cndmask_b32_e64 v58, v240, v58, s[22:23]
	v_cmp_gt_u32_e64 s[22:23], s57, v128
	v_subrev_u32_e32 v128, 49, v0
	v_cmp_gt_u32_e64 s[24:25], s57, v128
	v_subrev_u32_e32 v128, 18, v0
	s_nop 0
	v_cndmask_b32_e64 v59, v240, v59, s[24:25]
	v_cmp_gt_u32_e64 s[24:25], s57, v128
	v_subrev_u32_e32 v128, 50, v0
	v_cmp_gt_u32_e64 s[26:27], s57, v128
	v_subrev_u32_e32 v128, 19, v0
	s_nop 0
	v_cndmask_b32_e64 v60, v240, v60, s[26:27]
	v_cmp_gt_u32_e64 s[26:27], s57, v128
	v_subrev_u32_e32 v128, 51, v0
	v_cmp_gt_u32_e64 s[28:29], s57, v128
	v_subrev_u32_e32 v128, 24, v0
	s_nop 0
	v_cndmask_b32_e64 v61, v240, v61, s[28:29]
	v_cmp_gt_u32_e64 s[28:29], s57, v128
	v_subrev_u32_e32 v128, 56, v0
	v_cmp_gt_u32_e64 s[30:31], s57, v128
	v_subrev_u32_e32 v128, 25, v0
	s_nop 0
	v_cndmask_b32_e64 v62, v240, v62, s[30:31]
	v_cmp_gt_u32_e64 s[30:31], s57, v128
	v_subrev_u32_e32 v128, 57, v0
	v_cmp_gt_u32_e64 s[34:35], s57, v128
	v_subrev_u32_e32 v128, 26, v0
	s_nop 0
	v_cndmask_b32_e64 v63, v240, v63, s[34:35]
	v_cmp_gt_u32_e64 s[34:35], s57, v128
	v_subrev_u32_e32 v128, 58, v0
	v_cmp_gt_u32_e64 s[36:37], s57, v128
	v_subrev_u32_e32 v128, 27, v0
	v_subrev_u32_e32 v0, 59, v0
	v_cndmask_b32_e64 v64, v240, v64, s[36:37]
	v_cmp_gt_u32_e64 s[36:37], s57, v128
	v_cmp_lt_u32_e64 s[38:39], s60, v0
	s_and_saveexec_b64 s[44:45], s[38:39]
	v_mov_b32_e32 v65, s61
	s_or_b64 exec, exec, s[44:45]
	v_cndmask_b32_e32 v34, v240, v34, vcc
	v_cndmask_b32_e64 v35, v240, v35, s[6:7]
	v_cndmask_b32_e64 v36, v240, v36, s[8:9]
	v_cndmask_b32_e64 v37, v240, v37, s[10:11]
	v_cndmask_b32_e64 v38, v240, v38, s[12:13]
	v_cndmask_b32_e64 v39, v240, v39, s[14:15]
	v_cndmask_b32_e64 v40, v240, v40, s[16:17]
	v_cndmask_b32_e64 v41, v240, v41, s[18:19]
	v_cndmask_b32_e64 v42, v240, v42, s[20:21]
	v_cndmask_b32_e64 v43, v240, v43, s[22:23]
	v_cndmask_b32_e64 v44, v240, v44, s[24:25]
	v_cndmask_b32_e64 v45, v240, v45, s[26:27]
	v_cndmask_b32_e64 v46, v240, v46, s[28:29]
	v_cndmask_b32_e64 v47, v240, v47, s[30:31]
	v_cndmask_b32_e64 v48, v240, v48, s[34:35]
	v_cndmask_b32_e64 v49, v240, v49, s[36:37]

.LBB0_3640:
	s_add_i32 s55, s7, 0
	s_add_i32 s4, s55, s51
	v_add3_u32 v14, s4, v136, v137
	ds_read_b128 v[2:5], v14
	ds_read_b128 v[6:9], v14 offset:512
	ds_read_b128 v[10:13], v14 offset:2048
	ds_read_b128 v[142:145], v14 offset:2560
	s_lshl_b32 s4, s6, 6
	v_readfirstlane_b32 s5, v134
	s_or_b32 s6, s4, 63
	s_cmp_le_i32 s6, s5
	s_cselect_b64 s[6:7], -1, 0
	s_waitcnt lgkmcnt(3)
	v_mfma_f32_32x32x16_bf16 v[96:111], v[2:5], v[112:115], 0
	s_add_i32 s5, s5, 0xf000001f
	s_cmp_gt_i32 s4, s5
	s_cselect_b64 s[8:9], -1, 0
	s_and_b64 s[6:7], s[6:7], s[8:9]
	s_and_b64 vcc, exec, s[6:7]
	s_waitcnt lgkmcnt(2)
	v_mfma_f32_32x32x16_bf16 v[80:95], v[6:9], v[112:115], 0
	ds_read_b128 v[2:5], v14 offset:4096
	ds_read_b128 v[6:9], v14 offset:4608
	s_waitcnt lgkmcnt(3)
	v_mfma_f32_32x32x16_bf16 v[96:111], v[10:13], v[116:119], v[96:111]
	s_waitcnt lgkmcnt(2)
	v_mfma_f32_32x32x16_bf16 v[80:95], v[142:145], v[116:119], v[80:95]
	ds_read_b128 v[10:13], v14 offset:6144
	ds_read_b128 v[142:145], v14 offset:6656
	s_waitcnt lgkmcnt(3)
	v_mfma_f32_32x32x16_bf16 v[96:111], v[2:5], v[120:123], v[96:111]
	s_waitcnt lgkmcnt(2)
	v_mfma_f32_32x32x16_bf16 v[80:95], v[6:9], v[120:123], v[80:95]
	s_waitcnt lgkmcnt(1)
	v_mfma_f32_32x32x16_bf16 v[96:111], v[10:13], v[124:127], v[96:111]
	s_waitcnt lgkmcnt(0)
	v_mfma_f32_32x32x16_bf16 v[80:95], v[142:145], v[124:127], v[80:95]
	s_cbranch_vccnz .LBB0_3644
	v_or_b32_e32 v2, s4, v129
	v_sub_u32_e32 v2, v134, v2
	v_subrev_u32_e32 v3, 32, v2
	v_cmp_gt_u32_e64 s[4:5], s1, v3
	v_add_u32_e32 v3, -1, v2
	v_cmp_gt_u32_e32 vcc, s1, v2
	s_nop 4
	v_cndmask_b32_e64 v80, v240, v80, s[4:5]
	v_cmp_gt_u32_e64 s[4:5], s1, v3
	v_subrev_u32_e32 v3, 33, v2
	v_cmp_gt_u32_e64 s[6:7], s1, v3
	v_add_u32_e32 v3, -2, v2
	s_brev_b32 s36, -16
	v_cndmask_b32_e64 v81, v240, v81, s[6:7]
	v_cmp_gt_u32_e64 s[6:7], s1, v3
	v_subrev_u32_e32 v3, 34, v2
	v_cmp_gt_u32_e64 s[8:9], s1, v3
	v_add_u32_e32 v3, -3, v2
	s_nop 0
	v_cndmask_b32_e64 v82, v240, v82, s[8:9]
	v_cmp_gt_u32_e64 s[8:9], s1, v3
	v_subrev_u32_e32 v3, 35, v2
	v_cmp_gt_u32_e64 s[10:11], s1, v3
	v_add_u32_e32 v3, -8, v2
	s_nop 0
	v_cndmask_b32_e64 v83, v240, v83, s[10:11]
	v_cmp_gt_u32_e64 s[10:11], s1, v3
	v_subrev_u32_e32 v3, 40, v2
	v_cmp_gt_u32_e64 s[12:13], s1, v3
	v_add_u32_e32 v3, -9, v2
	s_nop 0
	v_cndmask_b32_e64 v84, v240, v84, s[12:13]
	v_cmp_gt_u32_e64 s[12:13], s1, v3
	v_subrev_u32_e32 v3, 41, v2
	v_cmp_gt_u32_e64 s[14:15], s1, v3
	v_add_u32_e32 v3, -10, v2
	s_nop 0
	v_cndmask_b32_e64 v85, v240, v85, s[14:15]
	v_cmp_gt_u32_e64 s[14:15], s1, v3
	v_subrev_u32_e32 v3, 42, v2
	v_cmp_gt_u32_e64 s[16:17], s1, v3
	v_add_u32_e32 v3, -11, v2
	s_nop 0
	v_cndmask_b32_e64 v86, v240, v86, s[16:17]
	v_cmp_gt_u32_e64 s[16:17], s1, v3
	v_subrev_u32_e32 v3, 43, v2
	v_cmp_gt_u32_e64 s[18:19], s1, v3
	v_add_u32_e32 v3, -16, v2
	s_nop 0
	v_cndmask_b32_e64 v87, v240, v87, s[18:19]
	v_cmp_gt_u32_e64 s[18:19], s1, v3
	v_subrev_u32_e32 v3, 48, v2
	v_cmp_gt_u32_e64 s[20:21], s1, v3
	v_subrev_u32_e32 v3, 17, v2
	s_nop 0
	v_cndmask_b32_e64 v88, v240, v88, s[20:21]
	v_cmp_gt_u32_e64 s[20:21], s1, v3
	v_subrev_u32_e32 v3, 49, v2
	v_cmp_gt_u32_e64 s[22:23], s1, v3
	v_subrev_u32_e32 v3, 18, v2
	s_nop 0
	v_cndmask_b32_e64 v89, v240, v89, s[22:23]
	v_cmp_gt_u32_e64 s[22:23], s1, v3
	v_subrev_u32_e32 v3, 50, v2
	v_cmp_gt_u32_e64 s[24:25], s1, v3
	v_subrev_u32_e32 v3, 19, v2
	s_nop 0
	v_cndmask_b32_e64 v90, v240, v90, s[24:25]
	v_cmp_gt_u32_e64 s[24:25], s1, v3
	v_subrev_u32_e32 v3, 51, v2
	v_cmp_gt_u32_e64 s[26:27], s1, v3
	v_subrev_u32_e32 v3, 24, v2
	s_nop 0
	v_cndmask_b32_e64 v91, v240, v91, s[26:27]
	v_cmp_gt_u32_e64 s[26:27], s1, v3
	v_subrev_u32_e32 v3, 56, v2
	v_cmp_gt_u32_e64 s[28:29], s1, v3
	v_subrev_u32_e32 v3, 25, v2
	s_nop 0
	v_cndmask_b32_e64 v92, v240, v92, s[28:29]
	v_cmp_gt_u32_e64 s[28:29], s1, v3
	v_subrev_u32_e32 v3, 57, v2
	v_cmp_gt_u32_e64 s[30:31], s1, v3
	v_subrev_u32_e32 v3, 26, v2
	s_nop 0
	v_cndmask_b32_e64 v93, v240, v93, s[30:31]
	v_cmp_gt_u32_e64 s[30:31], s1, v3
	v_subrev_u32_e32 v3, 58, v2
	v_cmp_gt_u32_e64 s[34:35], s1, v3
	v_subrev_u32_e32 v3, 27, v2
	v_subrev_u32_e32 v2, 59, v2
	v_cndmask_b32_e64 v94, v240, v94, s[34:35]
	v_cmp_gt_u32_e64 s[34:35], s1, v3
	v_cmp_lt_u32_e64 s[36:37], s36, v2
	s_and_saveexec_b64 s[46:47], s[36:37]
	v_mov_b32_e32 v95, s61
	s_or_b64 exec, exec, s[46:47]
	v_cndmask_b32_e32 v96, v240, v96, vcc
	v_cndmask_b32_e64 v97, v240, v97, s[4:5]
	v_cndmask_b32_e64 v98, v240, v98, s[6:7]
	v_cndmask_b32_e64 v99, v240, v99, s[8:9]
	v_cndmask_b32_e64 v100, v240, v100, s[10:11]
	v_cndmask_b32_e64 v101, v240, v101, s[12:13]
	v_cndmask_b32_e64 v102, v240, v102, s[14:15]
	v_cndmask_b32_e64 v103, v240, v103, s[16:17]
	v_cndmask_b32_e64 v104, v240, v104, s[18:19]
	v_cndmask_b32_e64 v105, v240, v105, s[20:21]
	v_cndmask_b32_e64 v106, v240, v106, s[22:23]
	v_cndmask_b32_e64 v107, v240, v107, s[24:25]
	v_cndmask_b32_e64 v108, v240, v108, s[26:27]
	v_cndmask_b32_e64 v109, v240, v109, s[28:29]
	v_cndmask_b32_e64 v110, v240, v110, s[30:31]
	v_cndmask_b32_e64 v111, v240, v111, s[34:35]

.LBB0_3736:
	s_add_i32 s92, s9, 0
	v_add3_u32 v111, s92, v162, v163
	ds_read_b128 v[66:69], v111
	ds_read_b128 v[70:73], v111 offset:512
	ds_read_b128 v[106:109], v111 offset:2048
	ds_read_b128 v[164:167], v111 offset:2560
	s_lshl_b32 s10, s8, 6
	v_readfirstlane_b32 s9, v156
	s_waitcnt lgkmcnt(3)
	v_mfma_f32_32x32x16_bf16 v[82:97], v[66:69], v[112:115], 0
	s_waitcnt lgkmcnt(2)
	v_mfma_f32_32x32x16_bf16 v[66:81], v[70:73], v[112:115], 0
	ds_read_b128 v[168:171], v111 offset:4096
	ds_read_b128 v[172:175], v111 offset:4608
	s_waitcnt lgkmcnt(3)
	v_mfma_f32_32x32x16_bf16 v[82:97], v[106:109], v[116:119], v[82:97]
	s_waitcnt lgkmcnt(2)
	v_mfma_f32_32x32x16_bf16 v[66:81], v[164:167], v[116:119], v[66:81]
	ds_read_b128 v[106:109], v111 offset:6144
	ds_read_b128 v[164:167], v111 offset:6656
	s_waitcnt lgkmcnt(3)
	v_mfma_f32_32x32x16_bf16 v[82:97], v[168:171], v[120:123], v[82:97]
	s_waitcnt lgkmcnt(2)
	v_mfma_f32_32x32x16_bf16 v[66:81], v[172:175], v[120:123], v[66:81]
	ds_read_b128 v[168:171], v111 offset:8192
	ds_read_b128 v[172:175], v111 offset:8704
	s_waitcnt lgkmcnt(3)
	v_mfma_f32_32x32x16_bf16 v[82:97], v[106:109], v[124:127], v[82:97]
	s_waitcnt lgkmcnt(2)
	v_mfma_f32_32x32x16_bf16 v[66:81], v[164:167], v[124:127], v[66:81]
	ds_read_b128 v[106:109], v111 offset:10240
	ds_read_b128 v[164:167], v111 offset:10752
	s_waitcnt lgkmcnt(3)
	v_mfma_f32_32x32x16_bf16 v[82:97], v[168:171], v[128:131], v[82:97]
	s_waitcnt lgkmcnt(2)
	v_mfma_f32_32x32x16_bf16 v[66:81], v[172:175], v[128:131], v[66:81]
	ds_read_b128 v[168:171], v111 offset:12288
	ds_read_b128 v[172:175], v111 offset:12800
	s_waitcnt lgkmcnt(3)
	v_mfma_f32_32x32x16_bf16 v[82:97], v[106:109], v[132:135], v[82:97]
	s_waitcnt lgkmcnt(2)
	v_mfma_f32_32x32x16_bf16 v[66:81], v[164:167], v[132:135], v[66:81]
	ds_read_b128 v[106:109], v111 offset:14336
	ds_read_b128 v[164:167], v111 offset:14848
	s_waitcnt lgkmcnt(3)
	v_mfma_f32_32x32x16_bf16 v[82:97], v[168:171], v[136:139], v[82:97]
	s_waitcnt lgkmcnt(2)
	v_mfma_f32_32x32x16_bf16 v[66:81], v[172:175], v[136:139], v[66:81]
	s_waitcnt lgkmcnt(1)
	v_mfma_f32_32x32x16_bf16 v[82:97], v[106:109], v[140:143], v[82:97]
	v_lshrrev_b32_e32 v106, s8, v110
	s_or_b32 s8, s10, 63
	s_cmp_gt_i32 s8, s9
	v_and_b32_e32 v106, 1, v106
	s_cselect_b64 s[8:9], -1, 0
	v_cmp_eq_u32_e64 s[6:7], 1, v106
	s_and_b64 vcc, exec, s[8:9]
	s_waitcnt lgkmcnt(0)
	v_mfma_f32_32x32x16_bf16 v[66:81], v[164:167], v[140:143], v[66:81]
	s_cbranch_vccnz .LBB0_3738
	v_cndmask_b32_e64 v106, 0, 1, s[6:7]
	v_cmp_ne_u32_e32 vcc, 0, v106
	s_cmp_lg_u64 vcc, exec
	s_cselect_b64 s[8:9], -1, 0

.LBB0_3761:
	s_add_i32 s42, s8, 0
	v_add3_u32 v0, s42, v162, v163
	ds_read_b128 v[2:5], v0
	ds_read_b128 v[6:9], v0 offset:512
	ds_read_b128 v[10:13], v0 offset:2048
	ds_read_b128 v[166:169], v0 offset:2560
	s_lshl_b32 s6, s9, 6
	v_readfirstlane_b32 s7, v156
	s_or_b32 s8, s6, 63
	s_cmp_le_i32 s8, s7
	s_cselect_b64 s[8:9], -1, 0
	s_waitcnt lgkmcnt(3)
	v_mfma_f32_32x32x16_bf16 v[96:111], v[2:5], v[112:115], 0
	s_addk_i32 s7, 0xfe1f
	s_cmp_gt_i32 s6, s7
	s_cselect_b64 s[10:11], -1, 0
	s_and_b64 s[8:9], s[8:9], s[10:11]
	s_and_b64 vcc, exec, s[8:9]
	s_waitcnt lgkmcnt(2)
	v_mfma_f32_32x32x16_bf16 v[80:95], v[6:9], v[112:115], 0
	ds_read_b128 v[2:5], v0 offset:4096
	ds_read_b128 v[6:9], v0 offset:4608
	s_waitcnt lgkmcnt(3)
	v_mfma_f32_32x32x16_bf16 v[96:111], v[10:13], v[116:119], v[96:111]
	s_waitcnt lgkmcnt(2)
	v_mfma_f32_32x32x16_bf16 v[80:95], v[166:169], v[116:119], v[80:95]
	ds_read_b128 v[10:13], v0 offset:6144
	ds_read_b128 v[166:169], v0 offset:6656
	s_waitcnt lgkmcnt(3)
	v_mfma_f32_32x32x16_bf16 v[96:111], v[2:5], v[120:123], v[96:111]
	s_waitcnt lgkmcnt(2)
	v_mfma_f32_32x32x16_bf16 v[80:95], v[6:9], v[120:123], v[80:95]
	ds_read_b128 v[2:5], v0 offset:8192
	ds_read_b128 v[6:9], v0 offset:8704
	s_waitcnt lgkmcnt(3)
	v_mfma_f32_32x32x16_bf16 v[96:111], v[10:13], v[124:127], v[96:111]
	s_waitcnt lgkmcnt(2)
	v_mfma_f32_32x32x16_bf16 v[80:95], v[166:169], v[124:127], v[80:95]
	ds_read_b128 v[10:13], v0 offset:10240
	ds_read_b128 v[166:169], v0 offset:10752
	s_waitcnt lgkmcnt(3)
	v_mfma_f32_32x32x16_bf16 v[96:111], v[2:5], v[128:131], v[96:111]
	s_waitcnt lgkmcnt(2)
	v_mfma_f32_32x32x16_bf16 v[80:95], v[6:9], v[128:131], v[80:95]
	ds_read_b128 v[2:5], v0 offset:12288
	ds_read_b128 v[6:9], v0 offset:12800
	s_waitcnt lgkmcnt(3)
	v_mfma_f32_32x32x16_bf16 v[96:111], v[10:13], v[132:135], v[96:111]
	s_waitcnt lgkmcnt(2)
	v_mfma_f32_32x32x16_bf16 v[80:95], v[166:169], v[132:135], v[80:95]
	ds_read_b128 v[10:13], v0 offset:14336
	ds_read_b128 v[166:169], v0 offset:14848
	s_waitcnt lgkmcnt(3)
	v_mfma_f32_32x32x16_bf16 v[96:111], v[2:5], v[136:139], v[96:111]
	s_waitcnt lgkmcnt(2)
	v_mfma_f32_32x32x16_bf16 v[80:95], v[6:9], v[136:139], v[80:95]
	s_waitcnt lgkmcnt(1)
	v_mfma_f32_32x32x16_bf16 v[96:111], v[10:13], v[140:143], v[96:111]
	s_waitcnt lgkmcnt(0)
	v_mfma_f32_32x32x16_bf16 v[80:95], v[166:169], v[140:143], v[80:95]
	s_cbranch_vccnz .LBB0_3765
	v_or_b32_e32 v0, s6, v161
	v_sub_u32_e32 v0, v156, v0
	v_subrev_u32_e32 v2, 32, v0
	v_cmp_gt_u32_e64 s[6:7], s89, v2
	v_add_u32_e32 v2, -1, v0
	v_cmp_gt_u32_e32 vcc, s89, v0
	s_nop 4
	v_cndmask_b32_e64 v80, v240, v80, s[6:7]
	v_cmp_gt_u32_e64 s[6:7], s89, v2
	v_subrev_u32_e32 v2, 33, v0
	v_cmp_gt_u32_e64 s[8:9], s89, v2
	v_add_u32_e32 v2, -2, v0
	s_movk_i32 s38, 0x1ff
	v_cndmask_b32_e64 v81, v240, v81, s[8:9]
	v_cmp_gt_u32_e64 s[8:9], s89, v2
	v_subrev_u32_e32 v2, 34, v0
	v_cmp_gt_u32_e64 s[10:11], s89, v2
	v_add_u32_e32 v2, -3, v0
	s_nop 0
	v_cndmask_b32_e64 v82, v240, v82, s[10:11]
	v_cmp_gt_u32_e64 s[10:11], s89, v2
	v_subrev_u32_e32 v2, 35, v0
	v_cmp_gt_u32_e64 s[12:13], s89, v2
	v_add_u32_e32 v2, -8, v0
	s_nop 0
	v_cndmask_b32_e64 v83, v240, v83, s[12:13]
	v_cmp_gt_u32_e64 s[12:13], s89, v2
	v_subrev_u32_e32 v2, 40, v0
	v_cmp_gt_u32_e64 s[14:15], s89, v2
	v_add_u32_e32 v2, -9, v0
	s_nop 0
	v_cndmask_b32_e64 v84, v240, v84, s[14:15]
	v_cmp_gt_u32_e64 s[14:15], s89, v2
	v_subrev_u32_e32 v2, 41, v0
	v_cmp_gt_u32_e64 s[16:17], s89, v2
	v_add_u32_e32 v2, -10, v0
	s_nop 0
	v_cndmask_b32_e64 v85, v240, v85, s[16:17]
	v_cmp_gt_u32_e64 s[16:17], s89, v2
	v_subrev_u32_e32 v2, 42, v0
	v_cmp_gt_u32_e64 s[18:19], s89, v2
	v_add_u32_e32 v2, -11, v0
	s_nop 0
	v_cndmask_b32_e64 v86, v240, v86, s[18:19]
	v_cmp_gt_u32_e64 s[18:19], s89, v2
	v_subrev_u32_e32 v2, 43, v0
	v_cmp_gt_u32_e64 s[20:21], s89, v2
	v_add_u32_e32 v2, -16, v0
	s_nop 0
	v_cndmask_b32_e64 v87, v240, v87, s[20:21]
	v_cmp_gt_u32_e64 s[20:21], s89, v2
	v_subrev_u32_e32 v2, 48, v0
	v_cmp_gt_u32_e64 s[22:23], s89, v2
	v_subrev_u32_e32 v2, 17, v0
	s_nop 0
	v_cndmask_b32_e64 v88, v240, v88, s[22:23]
	v_cmp_gt_u32_e64 s[22:23], s89, v2
	v_subrev_u32_e32 v2, 49, v0
	v_cmp_gt_u32_e64 s[24:25], s89, v2
	v_subrev_u32_e32 v2, 18, v0
	s_nop 0
	v_cndmask_b32_e64 v89, v240, v89, s[24:25]
	v_cmp_gt_u32_e64 s[24:25], s89, v2
	v_subrev_u32_e32 v2, 50, v0
	v_cmp_gt_u32_e64 s[26:27], s89, v2
	v_subrev_u32_e32 v2, 19, v0
	s_nop 0
	v_cndmask_b32_e64 v90, v240, v90, s[26:27]
	v_cmp_gt_u32_e64 s[26:27], s89, v2
	v_subrev_u32_e32 v2, 51, v0
	v_cmp_gt_u32_e64 s[28:29], s89, v2
	v_subrev_u32_e32 v2, 24, v0
	s_nop 0
	v_cndmask_b32_e64 v91, v240, v91, s[28:29]
	v_cmp_gt_u32_e64 s[28:29], s89, v2
	v_subrev_u32_e32 v2, 56, v0
	v_cmp_gt_u32_e64 s[30:31], s89, v2
	v_subrev_u32_e32 v2, 25, v0
	s_nop 0
	v_cndmask_b32_e64 v92, v240, v92, s[30:31]
	v_cmp_gt_u32_e64 s[30:31], s89, v2
	v_subrev_u32_e32 v2, 57, v0
	v_cmp_gt_u32_e64 s[34:35], s89, v2
	v_subrev_u32_e32 v2, 26, v0
	s_nop 0
	v_cndmask_b32_e64 v93, v240, v93, s[34:35]
	v_cmp_gt_u32_e64 s[34:35], s89, v2
	v_subrev_u32_e32 v2, 58, v0
	v_cmp_gt_u32_e64 s[36:37], s89, v2
	v_subrev_u32_e32 v2, 27, v0
	v_subrev_u32_e32 v0, 59, v0
	v_cndmask_b32_e64 v94, v240, v94, s[36:37]
	v_cmp_gt_u32_e64 s[36:37], s89, v2
	v_cmp_lt_u32_e64 s[38:39], s38, v0
	s_and_saveexec_b64 s[40:41], s[38:39]
	v_mov_b32_e32 v95, s61
	s_or_b64 exec, exec, s[40:41]
	v_cndmask_b32_e32 v96, v240, v96, vcc
	v_cndmask_b32_e64 v97, v240, v97, s[6:7]
	v_cndmask_b32_e64 v98, v240, v98, s[8:9]
	v_cndmask_b32_e64 v99, v240, v99, s[10:11]
	v_cndmask_b32_e64 v100, v240, v100, s[12:13]
	v_cndmask_b32_e64 v101, v240, v101, s[14:15]
	v_cndmask_b32_e64 v102, v240, v102, s[16:17]
	v_cndmask_b32_e64 v103, v240, v103, s[18:19]
	v_cndmask_b32_e64 v104, v240, v104, s[20:21]
	v_cndmask_b32_e64 v105, v240, v105, s[22:23]
	v_cndmask_b32_e64 v106, v240, v106, s[24:25]
	v_cndmask_b32_e64 v107, v240, v107, s[26:27]
	v_cndmask_b32_e64 v108, v240, v108, s[28:29]
	v_cndmask_b32_e64 v109, v240, v109, s[30:31]
	v_cndmask_b32_e64 v110, v240, v110, s[34:35]
	v_cndmask_b32_e64 v111, v240, v111, s[36:37]

.LBB0_4958:
	s_add_i32 s18, s27, 0
	v_add3_u32 v137, s18, v148, v149
	ds_read_b128 v[66:69], v137
	ds_read_b128 v[70:73], v137 offset:512
	ds_read_b128 v[152:155], v137 offset:2048
	ds_read_b128 v[156:159], v137 offset:2560
	v_cmp_eq_f32_e32 vcc, 0, v135
	s_cmp_eq_u64 vcc, exec
	s_waitcnt lgkmcnt(3)
	v_mfma_f32_32x32x16_bf16 v[82:97], v[66:69], v[98:101], 0
	s_waitcnt lgkmcnt(2)
	v_mfma_f32_32x32x16_bf16 v[66:81], v[70:73], v[98:101], 0
	ds_read_b128 v[160:163], v137 offset:4096
	ds_read_b128 v[164:167], v137 offset:4608
	s_waitcnt lgkmcnt(3)
	v_mfma_f32_32x32x16_bf16 v[82:97], v[152:155], v[102:105], v[82:97]
	s_waitcnt lgkmcnt(2)
	v_mfma_f32_32x32x16_bf16 v[66:81], v[156:159], v[102:105], v[66:81]
	ds_read_b128 v[152:155], v137 offset:6144
	ds_read_b128 v[156:159], v137 offset:6656
	s_waitcnt lgkmcnt(3)
	v_mfma_f32_32x32x16_bf16 v[82:97], v[160:163], v[106:109], v[82:97]
	s_waitcnt lgkmcnt(2)
	v_mfma_f32_32x32x16_bf16 v[66:81], v[164:167], v[106:109], v[66:81]
	ds_read_b128 v[160:163], v137 offset:8192
	ds_read_b128 v[164:167], v137 offset:8704
	s_waitcnt lgkmcnt(3)
	v_mfma_f32_32x32x16_bf16 v[82:97], v[152:155], v[110:113], v[82:97]
	s_waitcnt lgkmcnt(2)
	v_mfma_f32_32x32x16_bf16 v[66:81], v[156:159], v[110:113], v[66:81]
	ds_read_b128 v[152:155], v137 offset:10240
	ds_read_b128 v[156:159], v137 offset:10752
	s_waitcnt lgkmcnt(3)
	v_mfma_f32_32x32x16_bf16 v[82:97], v[160:163], v[114:117], v[82:97]
	s_waitcnt lgkmcnt(2)
	v_mfma_f32_32x32x16_bf16 v[66:81], v[164:167], v[114:117], v[66:81]
	ds_read_b128 v[160:163], v137 offset:12288
	ds_read_b128 v[164:167], v137 offset:12800
	s_waitcnt lgkmcnt(3)
	v_mfma_f32_32x32x16_bf16 v[82:97], v[152:155], v[118:121], v[82:97]
	s_waitcnt lgkmcnt(2)
	v_mfma_f32_32x32x16_bf16 v[66:81], v[156:159], v[118:121], v[66:81]
	ds_read_b128 v[152:155], v137 offset:14336
	ds_read_b128 v[156:159], v137 offset:14848
	s_waitcnt lgkmcnt(3)
	v_mfma_f32_32x32x16_bf16 v[82:97], v[160:163], v[122:125], v[82:97]
	s_waitcnt lgkmcnt(2)
	v_mfma_f32_32x32x16_bf16 v[66:81], v[164:167], v[122:125], v[66:81]
	s_waitcnt lgkmcnt(1)
	v_mfma_f32_32x32x16_bf16 v[82:97], v[152:155], v[126:129], v[82:97]
	s_waitcnt lgkmcnt(0)
	v_mfma_f32_32x32x16_bf16 v[66:81], v[156:159], v[126:129], v[66:81]
	s_nop 10
	v_max_f32_e32 v137, v83, v83
	v_max_f32_e32 v139, v82, v82
	v_max_f32_e32 v137, v139, v137
	v_max3_f32 v139, v84, v85, v67
	v_max3_f32 v137, v137, v66, v68
	v_max3_f32 v137, v137, v69, v86
	v_max3_f32 v139, v139, v88, v89
	v_max3_f32 v137, v137, v87, v70
	v_max3_f32 v139, v139, v72, v73
	v_max3_f32 v137, v137, v71, v90
	v_max3_f32 v139, v139, v92, v93
	v_max3_f32 v137, v137, v91, v74
	v_max3_f32 v139, v139, v76, v77
	v_max3_f32 v137, v137, v75, v94
	v_max3_f32 v139, v139, v96, v97
	v_max3_f32 v137, v137, v95, v78
	v_max3_f32 v139, v139, v80, v81
	v_max3_f32 v137, v137, v79, v139
	v_mov_b32_e32 v139, v137
	s_nop 1
	v_permlane32_swap_b32_e32 v137, v139
	v_max_f32_e32 v139, v139, v139
	v_max_f32_e32 v137, v137, v137
	v_max_f32_e32 v137, v137, v139
	s_cbranch_scc1 .LBB0_4960
	v_sub_f32_e32 v97, v97, v135
	v_sub_f32_e32 v96, v96, v135
	v_sub_f32_e32 v95, v95, v135
	v_sub_f32_e32 v94, v94, v135
	v_sub_f32_e32 v93, v93, v135
	v_sub_f32_e32 v92, v92, v135
	v_sub_f32_e32 v91, v91, v135
	v_sub_f32_e32 v90, v90, v135
	v_sub_f32_e32 v89, v89, v135
	v_sub_f32_e32 v88, v88, v135
	v_sub_f32_e32 v87, v87, v135
	v_sub_f32_e32 v86, v86, v135
	v_sub_f32_e32 v85, v85, v135
	v_sub_f32_e32 v84, v84, v135
	v_sub_f32_e32 v83, v83, v135
	v_sub_f32_e32 v82, v82, v135
	v_sub_f32_e32 v81, v81, v135
	v_sub_f32_e32 v80, v80, v135
	v_sub_f32_e32 v79, v79, v135
	v_sub_f32_e32 v78, v78, v135
	v_sub_f32_e32 v77, v77, v135
	v_sub_f32_e32 v76, v76, v135
	v_sub_f32_e32 v75, v75, v135
	v_sub_f32_e32 v74, v74, v135
	v_sub_f32_e32 v73, v73, v135
	v_sub_f32_e32 v72, v72, v135
	v_sub_f32_e32 v71, v71, v135
	v_sub_f32_e32 v70, v70, v135
	v_sub_f32_e32 v69, v69, v135
	v_sub_f32_e32 v68, v68, v135
	v_sub_f32_e32 v67, v67, v135
	v_sub_f32_e32 v66, v66, v135
	v_sub_f32_e32 v137, v137, v135
